# stick-breaking attention: 32-query sub-blocks remapped across waves (0,1,2,3,7,6,5,4) so each SIMD's wave pair gets equal causal work
# speedup vs baseline: 1.0012x; 1.0012x over previous
; #define LAS __attribute__((address_space(3)))
; #define ATT_DEQ(ctrp, out) do { __syncthreads(); if (F.tid == 0) uslot[0] = __hip_atomic_fetch_add((ctrp), 1u, RLX_AGENT); __syncthreads(); (out) = (int)uslot[0] * 8 + qid; } while (0)
; template <int l>
; __device__ __forceinline__ void layer_phases(Frame& F, const XcdBarrier& bar, const int lo, const int hi) {
;     ...
;             const bf16* proj = (const bf16*)(ws + WS_PROJ); unsigned char* obuf = ws + WS_OBUF;
;             const float* gn = inptr<const float>(F, I_HNG) + (size_t)l * D;
;             LAS unsigned char* kvbuf = F.lds + RING_OFF; LAS float* ncum = (LAS float*)(F.lds + RING_OFF + 49152); att::lptr wl = F.lds + RING_OFF + 57344 + F.wave * 9216; LAS float* wsf = (LAS float*)(F.lds + WSF_OFF + F.wave * 256);
;             volatile LAS unsigned* uslot = (volatile LAS unsigned*)(F.lds + MISC_OFF + 64);
;             const int qid = blockIdx.x & 7;
;     ...
;             bf16* dstO = (bf16*)(ws + WS_DST_O); float* dstM = (float*)(ws + WS_DST_M);
;             if (rep == 0) { gu32* ctr = F.ctl + CW_AQ + ((l * 4 + 3) * 8 + qid) * 64;
;               for (;;) { int gi; ATT_DEQ(ctr, gi); if (gi >= 768) break;
;                   const int sl_ = gi >> 3, qb = sl_ / 12, bh = 12 * (gi & 7) + sl_ % 12;
;                   att::dil_a_unit(proj, dstO, dstM, F.ctl + CW_DA + ((l * 96 + bh) * 4 + (qb >> 1)) * 16, bh / 12, bh % 12, qb, wl, wsf, F.tid, F.wave); } }
;             if (ATT_ONLY < 0 || ATT_ONLY == 0) { gu32* ctr = F.ctl + CW_AQ + ((l * 4 + 0) * 8 + qid) * 64 + rep * 32;
;               for (;;) { int gi; ATT_DEQ(ctr, gi); if (gi >= 512) break;
;                   const int sl_ = gi >> 3, qb = 7 - sl_ / 8, bh = 8 * (gi & 7) + (sl_ & 7);
;                   att::sb_wave_unit(proj, gn, obuf, bh >> 3, bh & 7, 8 * qb + F.wave, wl, wsf, F.lane); } }
.LBB0_376:
	v_and_b32_e32 v1, 64, v216
	v_xor_b32_e32 v0, 1, v216
	v_add_u32_e32 v1, 64, v1
	v_cmp_lt_i32_e32 vcc, v0, v1
	s_lshl_b32 s6, s23, 22
	s_sub_i32 s20, 0x200, s23
	v_cndmask_b32_e32 v0, v216, v0, vcc
	v_lshlrev_b32_e32 v178, 2, v0
	s_add_u32 s89, s56, 0x51c00000
	v_ashrrev_i32_e32 v0, 5, v132
	s_addc_u32 s90, s57, 0
	s_lshl_b32 s12, s23, 20
	s_waitcnt vmcnt(1)
	v_lshlrev_b32_e32 v106, 2, v0
	s_add_u32 s21, s89, s6
	v_or_b32_e32 v1, v106, v126
	s_addc_u32 s23, s90, 0
	s_lshl_b32 s6, s24, 2
	v_lshl_add_u32 v107, v1, 6, v134
	v_ashrrev_i32_e32 v1, 3, v132
	s_add_u32 s6, s56, s6
	v_xor_b32_e32 v10, v1, v143
	v_xor_b32_e32 v11, v144, v1
	v_add_u32_e32 v12, 64, v132
	v_add_u32_e32 v14, 0x80, v132
	v_add_u32_e32 v16, 0xc0, v132
	v_and_b32_e32 v18, 0xffffffc, v1
	s_movk_i32 s16, 0x110
	v_or_b32_e32 v1, 3, v1
	s_addc_u32 s7, s57, 0
	v_lshlrev_b32_e32 v96, 3, v0
	v_lshl_add_u32 v3, v0, 9, s22
	v_xor_b32_e32 v4, v0, v128
	v_add_u32_e32 v5, 2, v0
	v_add_u32_e32 v7, 4, v0
	v_add_u32_e32 v0, 6, v0
	v_ashrrev_i32_e32 v12, 3, v12
	v_ashrrev_i32_e32 v14, 3, v14
	v_ashrrev_i32_e32 v16, 3, v16
	v_mul_lo_u32 v18, v18, s16
	v_lshlrev_b32_e32 v105, 2, v128
	v_mul_lo_u32 v1, v1, s16
	s_waitcnt vmcnt(0)
	v_ashrrev_i32_e32 v110, 1, v132
	s_add_u32 s14, s6, 0xc000
	v_mov_b32_e32 v113, 0
	v_and_b32_e32 v104, 48, v112
	v_lshl_add_u32 v6, v5, 9, s22
	v_xor_b32_e32 v5, v5, v128
	v_lshl_add_u32 v8, v7, 9, s22
	v_xor_b32_e32 v7, v7, v128
	v_lshl_add_u32 v9, v0, 9, s22
	v_xor_b32_e32 v0, v0, v128
	v_xor_b32_e32 v13, v12, v143
	v_xor_b32_e32 v12, v12, v144
	v_xor_b32_e32 v15, v14, v143
	v_xor_b32_e32 v14, v14, v144
	v_xor_b32_e32 v17, v16, v143
	v_xor_b32_e32 v16, v16, v144
	v_add3_u32 v108, s22, v18, v105
	v_add3_u32 v109, s22, v1, v105
	v_and_b32_e32 v1, 1, v132
	v_mul_lo_u32 v18, v110, s16
	s_addc_u32 s15, s7, 0
	v_add_u32_e32 v2, v133, v104
	v_lshlrev_b32_e32 v4, 4, v4
	v_lshlrev_b32_e32 v5, 4, v5
	v_lshlrev_b32_e32 v7, 4, v7
	v_lshlrev_b32_e32 v0, 4, v0
	v_cmp_gt_u32_e64 s[6:7], 32, v132
	v_lshlrev_b32_e32 v10, 4, v10
	v_lshlrev_b32_e32 v11, 6, v11
	v_lshlrev_b32_e32 v13, 4, v13
	v_lshlrev_b32_e32 v12, 6, v12
	v_lshlrev_b32_e32 v15, 4, v15
	v_lshlrev_b32_e32 v14, 6, v14
	v_lshlrev_b32_e32 v17, 4, v17
	v_lshlrev_b32_e32 v16, 6, v16
	v_add_u32_e32 v18, s22, v18
	v_lshlrev_b32_e32 v132, 7, v1
	v_mov_b32_e32 v133, v113
	s_sub_i32 s100, 11, s80
	s_cmp_lt_u32 s80, 4
	s_cselect_b32 s100, s80, s100
	s_lshl_b32 s25, s100, 5
	s_mov_b32 s13, 0
	s_add_i32 s24, s100, 56
	v_ashrrev_i32_e32 v97, 31, v96
	v_cmp_lt_i32_e64 s[8:9], v106, v128
	v_lshl_add_u32 v111, v110, 2, s86
	v_lshlrev_b32_e32 v134, 5, v1
	v_mov_b32_e32 v135, v113
	v_lshl_add_u64 v[136:137], s[10:11], 0, v[132:133]
	s_addk_i32 s25, 0x6c0
	s_add_i32 s26, 0, 0x21540
	s_lshl_b32 s27, s12, 1
	s_mov_b32 s28, 0xda24260
	v_mov_b32_e32 v114, 1.0
	v_add_u32_e32 v115, v18, v132
	v_mov_b32_e32 v116, 0x358637bd
	s_mov_b32 s29, 0xf800000
	v_mov_b32_e32 v117, 0x260
	v_add_u32_e32 v118, v154, v10
	v_add_u32_e32 v119, v2, v11
	v_add_u32_e32 v120, v154, v13
	v_add_u32_e32 v121, v2, v12
	v_add_u32_e32 v122, v154, v15
	v_add_u32_e32 v123, v2, v14
	v_add_u32_e32 v133, v154, v17
	v_add_u32_e32 v142, v2, v16
	v_add_u32_e32 v145, v3, v4
	v_add_u32_e32 v146, v6, v5
	v_add_u32_e32 v147, v8, v7
	v_add_u32_e32 v152, v9, v0
	s_and_saveexec_b64 s[98:99], s[0:1]
	v_mov_b32_e32 v239, 0
	v_mov_b32_e32 v240, 1
	global_atomic_add v238, v239, v240, s[14:15] sc0
	s_mov_b64 exec, s[98:99]
	s_branch .LBB0_379

; #define LAS __attribute__((address_space(3)))
; #define ATT_DEQ(ctrp, out) do { __syncthreads(); if (F.tid == 0) uslot[0] = __hip_atomic_fetch_add((ctrp), 1u, RLX_AGENT); __syncthreads(); (out) = (int)uslot[0] * 8 + qid; } while (0)
; template <int l>
; __device__ __forceinline__ void layer_phases(Frame& F, const XcdBarrier& bar, const int lo, const int hi) {
;     ...
;             const bf16* proj = (const bf16*)(ws + WS_PROJ); unsigned char* obuf = ws + WS_OBUF;
;             const float* gn = inptr<const float>(F, I_HNG) + (size_t)l * D;
;             LAS unsigned char* kvbuf = F.lds + RING_OFF; LAS float* ncum = (LAS float*)(F.lds + RING_OFF + 49152); att::lptr wl = F.lds + RING_OFF + 57344 + F.wave * 9216; LAS float* wsf = (LAS float*)(F.lds + WSF_OFF + F.wave * 256);
;             volatile LAS unsigned* uslot = (volatile LAS unsigned*)(F.lds + MISC_OFF + 64);
;             const int qid = blockIdx.x & 7;
;     ...
;             bf16* dstO = (bf16*)(ws + WS_DST_O); float* dstM = (float*)(ws + WS_DST_M);
;             if (rep == 0) { gu32* ctr = F.ctl + CW_AQ + ((l * 4 + 3) * 8 + qid) * 64;
;               for (;;) { int gi; ATT_DEQ(ctr, gi); if (gi >= 768) break;
;                   const int sl_ = gi >> 3, qb = sl_ / 12, bh = 12 * (gi & 7) + sl_ % 12;
;                   att::dil_a_unit(proj, dstO, dstM, F.ctl + CW_DA + ((l * 96 + bh) * 4 + (qb >> 1)) * 16, bh / 12, bh % 12, qb, wl, wsf, F.tid, F.wave); } }
;             if (ATT_ONLY < 0 || ATT_ONLY == 0) { gu32* ctr = F.ctl + CW_AQ + ((l * 4 + 0) * 8 + qid) * 64 + rep * 32;
;               for (;;) { int gi; ATT_DEQ(ctr, gi); if (gi >= 512) break;
;                   const int sl_ = gi >> 3, qb = 7 - sl_ / 8, bh = 8 * (gi & 7) + (sl_ & 7);
;                   att::sb_wave_unit(proj, gn, obuf, bh >> 3, bh & 7, 8 * qb + F.wave, wl, wsf, F.lane); } }
.LBB0_1286:
	v_and_b32_e32 v1, 64, v216
	v_xor_b32_e32 v0, 1, v216
	v_add_u32_e32 v1, 64, v1
	v_cmp_lt_i32_e32 vcc, v0, v1
	s_lshl_b32 s6, s23, 22
	s_sub_i32 s20, 0x200, s23
	v_cndmask_b32_e32 v0, v216, v0, vcc
	v_lshlrev_b32_e32 v178, 2, v0
	v_ashrrev_i32_e32 v0, 5, v132
	s_waitcnt vmcnt(3)
	v_lshlrev_b32_e32 v96, 3, v0
	s_waitcnt vmcnt(1)
	v_lshlrev_b32_e32 v106, 2, v0
	v_lshl_add_u32 v3, v0, 9, s22
	v_xor_b32_e32 v4, v0, v128
	v_add_u32_e32 v5, 2, v0
	v_add_u32_e32 v7, 4, v0
	v_add_u32_e32 v0, 6, v0
	v_lshl_add_u32 v9, v0, 9, s22
	v_xor_b32_e32 v0, v0, v128
	v_or_b32_e32 v1, v106, v126
	v_lshlrev_b32_e32 v10, 4, v0
	v_ashrrev_i32_e32 v0, 3, v132
	v_lshl_add_u32 v107, v1, 6, v134
	v_xor_b32_e32 v1, v0, v143
	v_lshlrev_b32_e32 v11, 4, v1
	v_xor_b32_e32 v1, v144, v0
	v_lshlrev_b32_e32 v12, 6, v1
	v_add_u32_e32 v1, 64, v132
	v_ashrrev_i32_e32 v1, 3, v1
	v_xor_b32_e32 v13, v1, v143
	v_xor_b32_e32 v1, v1, v144
	v_lshlrev_b32_e32 v14, 6, v1
	v_add_u32_e32 v1, 0x80, v132
	v_ashrrev_i32_e32 v1, 3, v1
	v_xor_b32_e32 v15, v1, v143
	v_xor_b32_e32 v1, v1, v144
	v_lshlrev_b32_e32 v16, 6, v1
	v_add_u32_e32 v1, 0xc0, v132
	v_ashrrev_i32_e32 v1, 3, v1
	s_add_u32 s88, s56, 0x51c00000
	v_xor_b32_e32 v17, v1, v143
	v_xor_b32_e32 v1, v1, v144
	s_addc_u32 s89, s57, 0
	s_lshl_b32 s12, s23, 20
	v_lshlrev_b32_e32 v18, 6, v1
	v_and_b32_e32 v1, 0xffffffc, v0
	s_movk_i32 s16, 0x110
	v_or_b32_e32 v0, 3, v0
	s_add_u32 s21, s88, s6
	v_lshlrev_b32_e32 v105, 2, v128
	v_mul_lo_u32 v0, v0, s16
	s_addc_u32 s23, s89, 0
	v_mov_b32_e32 v113, 0
	v_and_b32_e32 v104, 48, v112
	v_mul_lo_u32 v1, v1, s16
	s_waitcnt vmcnt(0)
	v_add3_u32 v109, s22, v0, v105
	v_ashrrev_i32_e32 v110, 1, v132
	v_and_b32_e32 v0, 1, v132
	s_add_u32 s14, s90, 0xe000
	v_add_u32_e32 v2, v133, v104
	v_lshl_add_u32 v6, v5, 9, s22
	v_xor_b32_e32 v5, v5, v128
	v_lshl_add_u32 v8, v7, 9, s22
	v_xor_b32_e32 v7, v7, v128
	v_cmp_gt_u32_e64 s[6:7], 32, v132
	v_add3_u32 v108, s22, v1, v105
	v_mul_lo_u32 v1, v110, s16
	v_lshlrev_b32_e32 v132, 7, v0
	v_mov_b32_e32 v133, v113
	s_addc_u32 s15, s91, 0
	v_lshlrev_b32_e32 v4, 4, v4
	v_lshlrev_b32_e32 v5, 4, v5
	v_lshlrev_b32_e32 v7, 4, v7
	v_lshlrev_b32_e32 v13, 4, v13
	v_lshlrev_b32_e32 v15, 4, v15
	v_lshlrev_b32_e32 v17, 4, v17
	v_add_u32_e32 v19, s22, v1
	v_lshlrev_b32_e32 v134, 5, v0
	v_lshl_add_u64 v[0:1], s[10:11], 0, v[132:133]
	s_mov_b64 s[10:11], 0x2000
	s_sub_i32 s100, 11, s80
	s_cmp_lt_u32 s80, 4
	s_cselect_b32 s100, s80, s100
	s_lshl_b32 s25, s100, 5
	s_mov_b32 s13, 0
	s_add_i32 s24, s100, 56
	v_ashrrev_i32_e32 v97, 31, v96
	v_cmp_lt_i32_e64 s[8:9], v106, v128
	v_lshl_add_u32 v111, v110, 2, s82
	v_mov_b32_e32 v135, v113
	v_lshl_add_u64 v[136:137], v[0:1], 0, s[10:11]
	s_addk_i32 s25, 0x6c0
	s_add_i32 s26, 0, 0x21540
	s_lshl_b32 s27, s12, 1
	s_mov_b32 s28, 0xda24260
	v_mov_b32_e32 v114, 1.0
	v_add_u32_e32 v115, v19, v132
	v_mov_b32_e32 v116, 0x358637bd
	s_mov_b32 s29, 0xf800000
	v_mov_b32_e32 v117, 0x260
	v_add_u32_e32 v118, v154, v11
	v_add_u32_e32 v119, v2, v12
	v_add_u32_e32 v120, v154, v13
	v_add_u32_e32 v121, v2, v14
	v_add_u32_e32 v122, v154, v15
	v_add_u32_e32 v123, v2, v16
	v_add_u32_e32 v133, v154, v17
	v_add_u32_e32 v142, v2, v18
	v_add_u32_e32 v145, v3, v4
	v_add_u32_e32 v146, v6, v5
	v_add_u32_e32 v147, v8, v7
	v_add_u32_e32 v152, v9, v10
	s_and_saveexec_b64 s[98:99], s[0:1]
	v_mov_b32_e32 v239, 0
	v_mov_b32_e32 v240, 1
	global_atomic_add v238, v239, v240, s[14:15] sc0
	s_mov_b64 exec, s[98:99]
	s_branch .LBB0_1289
